# v039 stack + XCD leaders no longer bump the (now unread) per-XCD generation word after the barrier release
# baseline (speedup 1.0000x reference)
.LBB0_220:
	s_ff1_i32_b64 s7, s[4:5]
	v_readlane_b32 s8, v2, s7
	s_add_i32 s6, s6, s8
	s_lshl_b64 s[8:9], 1, s7
	s_andn2_b64 s[4:5], s[4:5], s[8:9]
	s_cmp_lg_u64 s[4:5], 0
	s_cbranch_scc1 .LBB0_220
	v_mbcnt_lo_u32_b32 v2, exec_lo, 0
	v_mbcnt_hi_u32_b32 v2, exec_hi, v2
	v_cmp_eq_u32_e32 vcc, 0, v2
	s_and_saveexec_b64 s[4:5], vcc
	s_xor_b64 s[4:5], exec, s[4:5]
	s_cbranch_execz .LBB0_223
	v_mov_b32_e32 v2, s6
	v_readlane_b32 s6, v254, 16
	v_readlane_b32 s7, v254, 17
	s_nop 4
.LBB0_223:
	s_or_b64 exec, exec, s[4:5]
	s_waitcnt vmcnt(0)

.LBB0_336:
	s_ff1_i32_b64 s9, s[6:7]
	v_readlane_b32 s10, v2, s9
	s_lshl_b64 s[12:13], 1, s9
	s_add_i32 s8, s8, s10
	s_andn2_b64 s[6:7], s[6:7], s[12:13]
	s_cmp_lg_u64 s[6:7], 0
	s_cbranch_scc1 .LBB0_336
	v_mbcnt_lo_u32_b32 v2, exec_lo, 0
	v_mbcnt_hi_u32_b32 v2, exec_hi, v2
	v_cmp_eq_u32_e32 vcc, 0, v2
	s_and_saveexec_b64 s[6:7], vcc
	s_xor_b64 s[6:7], exec, s[6:7]
	s_cbranch_execz .LBB0_339
	v_mov_b32_e32 v2, s8
	v_readlane_b32 s8, v254, 16
	v_readlane_b32 s9, v254, 17
	s_nop 4
.LBB0_339:
	s_or_b64 exec, exec, s[6:7]
	s_waitcnt vmcnt(0)

.LBB0_407:
	s_ff1_i32_b64 s7, s[4:5]
	v_readlane_b32 s8, v2, s7
	s_add_i32 s6, s6, s8
	s_lshl_b64 s[8:9], 1, s7
	s_andn2_b64 s[4:5], s[4:5], s[8:9]
	s_cmp_lg_u64 s[4:5], 0
	s_cbranch_scc1 .LBB0_407
	v_mbcnt_lo_u32_b32 v2, exec_lo, 0
	v_mbcnt_hi_u32_b32 v2, exec_hi, v2
	v_cmp_eq_u32_e32 vcc, 0, v2
	s_and_saveexec_b64 s[4:5], vcc
	s_xor_b64 s[4:5], exec, s[4:5]
	s_cbranch_execz .LBB0_410
	v_mov_b32_e32 v2, s6
	v_readlane_b32 s6, v254, 16
	v_readlane_b32 s7, v254, 17
	s_nop 4
.LBB0_410:
	s_or_b64 exec, exec, s[4:5]
	s_waitcnt vmcnt(0)

.LBB0_562:
	s_ff1_i32_b64 s7, s[4:5]
	v_readlane_b32 s8, v2, s7
	s_add_i32 s6, s6, s8
	s_lshl_b64 s[8:9], 1, s7
	s_andn2_b64 s[4:5], s[4:5], s[8:9]
	s_cmp_lg_u64 s[4:5], 0
	s_cbranch_scc1 .LBB0_562
	v_mbcnt_lo_u32_b32 v2, exec_lo, 0
	v_mbcnt_hi_u32_b32 v2, exec_hi, v2
	v_cmp_eq_u32_e32 vcc, 0, v2
	s_and_saveexec_b64 s[4:5], vcc
	s_xor_b64 s[4:5], exec, s[4:5]
	s_cbranch_execz .LBB0_565
	v_mov_b32_e32 v2, s6
	v_readlane_b32 s6, v254, 16
	v_readlane_b32 s7, v254, 17
	s_nop 4
.LBB0_565:
	s_or_b64 exec, exec, s[4:5]
	s_waitcnt vmcnt(0)

.LBB0_666:
	s_ff1_i32_b64 s7, s[4:5]
	v_readlane_b32 s8, v2, s7
	s_add_i32 s6, s6, s8
	s_lshl_b64 s[8:9], 1, s7
	s_andn2_b64 s[4:5], s[4:5], s[8:9]
	s_cmp_lg_u64 s[4:5], 0
	s_cbranch_scc1 .LBB0_666
	v_mbcnt_lo_u32_b32 v2, exec_lo, 0
	v_mbcnt_hi_u32_b32 v2, exec_hi, v2
	v_cmp_eq_u32_e32 vcc, 0, v2
	s_and_saveexec_b64 s[4:5], vcc
	s_xor_b64 s[4:5], exec, s[4:5]
	s_cbranch_execz .LBB0_669
	v_mov_b32_e32 v2, s6
	v_readlane_b32 s6, v254, 16
	v_readlane_b32 s7, v254, 17
	s_nop 4
.LBB0_669:
	s_or_b64 exec, exec, s[4:5]
	s_waitcnt vmcnt(0)

.LBB0_751:
	s_ff1_i32_b64 s7, s[4:5]
	v_readlane_b32 s8, v2, s7
	s_add_i32 s6, s6, s8
	s_lshl_b64 s[8:9], 1, s7
	s_andn2_b64 s[4:5], s[4:5], s[8:9]
	s_cmp_lg_u64 s[4:5], 0
	s_cbranch_scc1 .LBB0_751
	v_mbcnt_lo_u32_b32 v2, exec_lo, 0
	v_mbcnt_hi_u32_b32 v2, exec_hi, v2
	v_cmp_eq_u32_e32 vcc, 0, v2
	s_and_saveexec_b64 s[4:5], vcc
	s_xor_b64 s[4:5], exec, s[4:5]
	s_cbranch_execz .LBB0_754
	v_mov_b32_e32 v2, s6
	v_readlane_b32 s6, v254, 16
	v_readlane_b32 s7, v254, 17
	s_nop 4
.LBB0_754:
	s_or_b64 exec, exec, s[4:5]
	s_waitcnt vmcnt(0)

.LBB0_914:
	s_ff1_i32_b64 s7, s[4:5]
	v_readlane_b32 s8, v2, s7
	s_add_i32 s6, s6, s8
	s_lshl_b64 s[8:9], 1, s7
	s_andn2_b64 s[4:5], s[4:5], s[8:9]
	s_cmp_lg_u64 s[4:5], 0
	s_cbranch_scc1 .LBB0_914
	v_mbcnt_lo_u32_b32 v2, exec_lo, 0
	v_mbcnt_hi_u32_b32 v2, exec_hi, v2
	v_cmp_eq_u32_e32 vcc, 0, v2
	s_and_saveexec_b64 s[4:5], vcc
	s_xor_b64 s[4:5], exec, s[4:5]
	s_cbranch_execz .LBB0_917
	v_mov_b32_e32 v2, s6
	v_readlane_b32 s6, v254, 16
	v_readlane_b32 s7, v254, 17
	s_nop 4
.LBB0_917:
	s_or_b64 exec, exec, s[4:5]
	s_waitcnt vmcnt(0)

.LBB0_996:
	s_ff1_i32_b64 s7, s[4:5]
	v_readlane_b32 s8, v2, s7
	s_add_i32 s6, s6, s8
	s_lshl_b64 s[8:9], 1, s7
	s_andn2_b64 s[4:5], s[4:5], s[8:9]
	s_cmp_lg_u64 s[4:5], 0
	s_cbranch_scc1 .LBB0_996
	v_mbcnt_lo_u32_b32 v2, exec_lo, 0
	v_mbcnt_hi_u32_b32 v2, exec_hi, v2
	v_cmp_eq_u32_e32 vcc, 0, v2
	s_and_saveexec_b64 s[4:5], vcc
	s_xor_b64 s[4:5], exec, s[4:5]
	s_cbranch_execz .LBB0_999
	v_mov_b32_e32 v2, s6
	v_readlane_b32 s6, v254, 16
	v_readlane_b32 s7, v254, 17
	s_nop 4
.LBB0_999:
	s_or_b64 exec, exec, s[4:5]
	s_waitcnt vmcnt(0)

.LBB0_1228:
	s_ff1_i32_b64 s7, s[4:5]
	v_readlane_b32 s8, v2, s7
	s_add_i32 s6, s6, s8
	s_lshl_b64 s[8:9], 1, s7
	s_andn2_b64 s[4:5], s[4:5], s[8:9]
	s_cmp_lg_u64 s[4:5], 0
	s_cbranch_scc1 .LBB0_1228
	v_mbcnt_lo_u32_b32 v2, exec_lo, 0
	v_mbcnt_hi_u32_b32 v2, exec_hi, v2
	v_cmp_eq_u32_e32 vcc, 0, v2
	s_and_saveexec_b64 s[4:5], vcc
	s_xor_b64 s[4:5], exec, s[4:5]
	s_cbranch_execz .LBB0_1231
	v_mov_b32_e32 v2, s6
	v_readlane_b32 s6, v254, 16
	v_readlane_b32 s7, v254, 17
	s_nop 4
.LBB0_1231:
	s_or_b64 exec, exec, s[4:5]
	s_waitcnt vmcnt(0)

.LBB0_1333:
	s_ff1_i32_b64 s7, s[4:5]
	v_readlane_b32 s8, v2, s7
	s_add_i32 s6, s6, s8
	s_lshl_b64 s[8:9], 1, s7
	s_andn2_b64 s[4:5], s[4:5], s[8:9]
	s_cmp_lg_u64 s[4:5], 0
	s_cbranch_scc1 .LBB0_1333
	v_mbcnt_lo_u32_b32 v2, exec_lo, 0
	v_mbcnt_hi_u32_b32 v2, exec_hi, v2
	v_cmp_eq_u32_e32 vcc, 0, v2
	s_and_saveexec_b64 s[4:5], vcc
	s_xor_b64 s[4:5], exec, s[4:5]
	s_cbranch_execz .LBB0_1336
	v_mov_b32_e32 v2, s6
	v_readlane_b32 s6, v254, 16
	v_readlane_b32 s7, v254, 17
	s_nop 4
.LBB0_1336:
	s_or_b64 exec, exec, s[4:5]
	s_waitcnt vmcnt(0)

.LBB0_1418:
	s_ff1_i32_b64 s7, s[4:5]
	v_readlane_b32 s8, v2, s7
	s_add_i32 s6, s6, s8
	s_lshl_b64 s[8:9], 1, s7
	s_andn2_b64 s[4:5], s[4:5], s[8:9]
	s_cmp_lg_u64 s[4:5], 0
	s_cbranch_scc1 .LBB0_1418
	v_mbcnt_lo_u32_b32 v2, exec_lo, 0
	v_mbcnt_hi_u32_b32 v2, exec_hi, v2
	v_cmp_eq_u32_e32 vcc, 0, v2
	s_and_saveexec_b64 s[4:5], vcc
	s_xor_b64 s[4:5], exec, s[4:5]
	s_cbranch_execz .LBB0_1421
	v_mov_b32_e32 v2, s6
	v_readlane_b32 s6, v254, 16
	v_readlane_b32 s7, v254, 17
	s_nop 4
.LBB0_1421:
	s_or_b64 exec, exec, s[4:5]
	s_waitcnt vmcnt(0)

.LBB0_1532:
	v_mov_b32_e32 v2, s6
	v_readlane_b32 s6, v254, 16
	v_readlane_b32 s7, v254, 17
	s_nop 4
	s_getpc_b64 s[98:99]
